# attention: first K/V tile requested together with the Q rows instead of after Q has arrived
# speedup vs baseline: 1.0001x; 1.0001x over previous
.LBB0_295:
	s_lshl_b32 s0, s35, 8
	s_and_b32 s28, s0, 0x700
	s_lshl_b32 s0, s35, 5
	s_and_b32 s26, s0, 0xfffff800
	s_ashr_i32 s27, s26, 31
	s_add_i32 s18, s28, s25
	s_lshl_b64 s[0:1], s[26:27], 13
	s_add_u32 s0, s12, s0
	s_addc_u32 s1, s13, s1
	s_lshl_b32 s27, s35, 4
	s_and_b32 s27, s27, 0x380
	s_lshl_b32 s29, s27, 1
	s_add_u32 s0, s0, s29
	v_or_b32_e32 v0, s18, v199
	s_addc_u32 s1, s1, 0
	v_lshlrev_b64 v[2:3], 13, v[0:1]
	v_lshl_add_u64 v[2:3], s[0:1], 0, v[2:3]
	v_mov_b32_e32 v197, v1
	v_lshl_add_u64 v[2:3], v[2:3], 0, v[196:197]
	global_load_dwordx4 v[6:9], v[2:3], off offset:224
	global_load_dwordx4 v[10:13], v[2:3], off
	global_load_dwordx4 v[14:17], v[2:3], off offset:32
	global_load_dwordx4 v[18:21], v[2:3], off offset:64
	global_load_dwordx4 v[22:25], v[2:3], off offset:96
	global_load_dwordx4 v[26:29], v[2:3], off offset:128
	global_load_dwordx4 v[30:33], v[2:3], off offset:160
	global_load_dwordx4 v[34:37], v[2:3], off offset:192
	s_lshr_b32 s28, s28, 6
	s_or_b32 s36, s28, 3
	v_mov_b32_e32 v201, v1
	v_lshl_add_u64 v[204:205], s[0:1], 0, v[200:201]
	v_lshl_or_b32 v248, s36, 19, v232
	v_add_u32_e32 v248, v248, v200
	v_add_u32_e32 v249, 0x1000, v248
	v_add_u32_e32 v251, 0x40000, v248
	global_load_dwordx4 v[240:243], v248, s[0:1] offset:2048
	global_load_dwordx4 v[244:247], v249, s[0:1]
	global_load_dwordx4 v[252:255], v251, s[0:1] offset:2048
	v_add_u32_e32 v249, 0x41000, v248
	global_load_dwordx4 v[236:239], v249, s[0:1]
	v_mov_b32_e32 v206, v0
	v_mov_b32_e32 v129, v0
	v_mov_b32_e32 v0, v1
	s_or_b32 s37, s18, 31
	v_mov_b32_e32 v197, 1.0
	s_mov_b32 s38, 0
	s_mov_b64 s[0:1], -1
	s_waitcnt vmcnt(11)
	v_lshlrev_b32_e32 v3, 16, v7
	s_waitcnt vmcnt(10)
	v_lshlrev_b32_e32 v38, 16, v13
	v_and_b32_e32 v39, 0xffff0000, v13
	v_lshlrev_b32_e32 v42, 16, v11
	v_and_b32_e32 v43, 0xffff0000, v11
	v_lshlrev_b32_e32 v44, 16, v10
	v_and_b32_e32 v45, 0xffff0000, v10
	v_lshlrev_b32_e32 v40, 16, v12
	v_and_b32_e32 v41, 0xffff0000, v12
	v_pk_mul_f32 v[72:73], v[38:39], v[38:39]
	v_pk_mul_f32 v[76:77], v[42:43], v[42:43]
	v_pk_mul_f32 v[78:79], v[44:45], v[44:45]
	v_pk_mul_f32 v[74:75], v[40:41], v[40:41]
	v_add_f32_e32 v72, v72, v73
	v_add_f32_e32 v73, v76, v77
	v_add_f32_e32 v76, v78, v79
	s_waitcnt vmcnt(9)
	v_lshlrev_b32_e32 v52, 16, v14
	v_and_b32_e32 v53, 0xffff0000, v14
	v_add_f32_e32 v73, v76, v73
	v_add_f32_e32 v74, v74, v75
	v_lshlrev_b32_e32 v50, 16, v15
	v_and_b32_e32 v51, 0xffff0000, v15
	v_pk_mul_f32 v[86:87], v[52:53], v[52:53]
	v_add_f32_e32 v73, v74, v73
	v_lshlrev_b32_e32 v48, 16, v16
	v_and_b32_e32 v49, 0xffff0000, v16
	v_pk_mul_f32 v[84:85], v[50:51], v[50:51]
	v_add_f32_e32 v72, v72, v73
	v_add_f32_e32 v73, v86, v87
	v_lshlrev_b32_e32 v46, 16, v17
	v_and_b32_e32 v47, 0xffff0000, v17
	v_pk_mul_f32 v[82:83], v[48:49], v[48:49]
	v_add_f32_e32 v72, v73, v72
	v_add_f32_e32 v73, v84, v85
	s_waitcnt vmcnt(8)
	v_lshlrev_b32_e32 v60, 16, v18
	v_and_b32_e32 v61, 0xffff0000, v18
	v_pk_mul_f32 v[80:81], v[46:47], v[46:47]
	v_add_f32_e32 v72, v73, v72
	v_add_f32_e32 v73, v82, v83
	v_lshlrev_b32_e32 v58, 16, v19
	v_and_b32_e32 v59, 0xffff0000, v19
	v_pk_mul_f32 v[94:95], v[60:61], v[60:61]
	v_add_f32_e32 v72, v73, v72
	v_add_f32_e32 v73, v80, v81
	v_lshlrev_b32_e32 v56, 16, v20
	v_and_b32_e32 v57, 0xffff0000, v20
	v_pk_mul_f32 v[92:93], v[58:59], v[58:59]
	v_add_f32_e32 v72, v73, v72
	v_add_f32_e32 v73, v94, v95
	v_lshlrev_b32_e32 v54, 16, v21
	v_and_b32_e32 v55, 0xffff0000, v21
	v_pk_mul_f32 v[90:91], v[56:57], v[56:57]
	v_add_f32_e32 v72, v73, v72
	v_add_f32_e32 v73, v92, v93
	s_waitcnt vmcnt(7)
	v_lshlrev_b32_e32 v68, 16, v22
	v_and_b32_e32 v69, 0xffff0000, v22
	v_pk_mul_f32 v[88:89], v[54:55], v[54:55]
	v_add_f32_e32 v72, v73, v72
	v_add_f32_e32 v73, v90, v91
	v_lshlrev_b32_e32 v66, 16, v23
	v_and_b32_e32 v67, 0xffff0000, v23
	v_pk_mul_f32 v[102:103], v[68:69], v[68:69]
	v_add_f32_e32 v72, v73, v72
	v_add_f32_e32 v73, v88, v89
	v_lshlrev_b32_e32 v64, 16, v24
	v_and_b32_e32 v65, 0xffff0000, v24
	v_pk_mul_f32 v[100:101], v[66:67], v[66:67]
	v_add_f32_e32 v72, v73, v72
	v_add_f32_e32 v73, v102, v103
	v_lshlrev_b32_e32 v2, 16, v6
	v_and_b32_e32 v7, 0xffff0000, v7
	v_and_b32_e32 v6, 0xffff0000, v6
	v_lshlrev_b32_e32 v5, 16, v9
	v_lshlrev_b32_e32 v4, 16, v8
	v_and_b32_e32 v9, 0xffff0000, v9
	v_and_b32_e32 v8, 0xffff0000, v8
	v_lshlrev_b32_e32 v62, 16, v25
	v_and_b32_e32 v63, 0xffff0000, v25
	v_pk_mul_f32 v[98:99], v[64:65], v[64:65]
	v_add_f32_e32 v72, v73, v72
	v_add_f32_e32 v73, v100, v101
	v_pk_mul_f32 v[14:15], v[6:7], v[6:7]
	v_pk_mul_f32 v[16:17], v[8:9], v[8:9]
	v_pk_mul_f32 v[96:97], v[62:63], v[62:63]
	s_waitcnt vmcnt(6)
	v_lshlrev_b32_e32 v114, 16, v26
	v_and_b32_e32 v115, 0xffff0000, v26
	v_add_f32_e32 v72, v73, v72
	v_add_f32_e32 v73, v98, v99
	v_lshlrev_b32_e32 v70, 16, v27
	v_and_b32_e32 v71, 0xffff0000, v27
	v_pk_fma_f32 v[108:109], v[2:3], v[2:3], v[14:15]
	v_pk_fma_f32 v[110:111], v[4:5], v[4:5], v[16:17]
	v_pk_mul_f32 v[116:117], v[114:115], v[114:115]
	s_waitcnt vmcnt(5)
	v_and_b32_e32 v15, 0xffff0000, v33
	v_and_b32_e32 v17, 0xffff0000, v32
	v_add_f32_e32 v72, v73, v72
	v_add_f32_e32 v73, v96, v97
	v_lshlrev_b32_e32 v12, 16, v28
	v_and_b32_e32 v13, 0xffff0000, v28
	v_pk_mul_f32 v[112:113], v[70:71], v[70:71]
	v_lshlrev_b32_e32 v14, 16, v33
	v_lshlrev_b32_e32 v16, 16, v32
	v_mov_b32_e32 v20, v15
	v_mov_b32_e32 v21, v17
	v_add_f32_e32 v72, v73, v72
	v_add_f32_e32 v73, v116, v117
	v_lshlrev_b32_e32 v10, 16, v29
	v_and_b32_e32 v11, 0xffff0000, v29
	v_pk_mul_f32 v[106:107], v[12:13], v[12:13]
	v_mov_b32_e32 v18, v14
	v_mov_b32_e32 v19, v16
	v_pk_mul_f32 v[20:21], v[20:21], v[20:21]
	v_add_f32_e32 v72, v73, v72
	v_add_f32_e32 v73, v112, v113
	v_pk_mul_f32 v[104:105], v[10:11], v[10:11]
	v_pk_fma_f32 v[32:33], v[18:19], v[18:19], v[20:21]
	v_lshlrev_b32_e32 v24, 16, v30
	v_and_b32_e32 v25, 0xffff0000, v30
	s_waitcnt vmcnt(4)
	v_and_b32_e32 v19, 0xffff0000, v37
	v_and_b32_e32 v21, 0xffff0000, v36
	v_add_f32_e32 v72, v73, v72
	v_add_f32_e32 v73, v106, v107
	v_lshlrev_b32_e32 v22, 16, v31
	v_and_b32_e32 v23, 0xffff0000, v31
	v_pk_mul_f32 v[30:31], v[24:25], v[24:25]
	v_lshlrev_b32_e32 v18, 16, v37
	v_lshlrev_b32_e32 v20, 16, v36
	v_mov_b32_e32 v28, v19
	v_mov_b32_e32 v29, v21
	v_add_f32_e32 v72, v73, v72
	v_add_f32_e32 v73, v104, v105
	v_pk_mul_f32 v[118:119], v[22:23], v[22:23]
	v_mov_b32_e32 v26, v18
	v_mov_b32_e32 v27, v20
	v_pk_mul_f32 v[28:29], v[28:29], v[28:29]
	v_add_f32_e32 v72, v73, v72
	v_add_f32_e32 v30, v30, v31
	v_pk_fma_f32 v[36:37], v[26:27], v[26:27], v[28:29]
	v_and_b32_e32 v27, 0xffff0000, v35
	v_and_b32_e32 v29, 0xffff0000, v34
	v_add_f32_e32 v30, v30, v72
	v_add_f32_e32 v31, v118, v119
	v_lshlrev_b32_e32 v26, 16, v35
	v_lshlrev_b32_e32 v28, 16, v34
	v_mov_b32_e32 v120, v27
	v_mov_b32_e32 v121, v29
	v_add_f32_e32 v30, v31, v30
	v_mov_b32_e32 v34, v26
	v_mov_b32_e32 v35, v28
	v_pk_mul_f32 v[120:121], v[120:121], v[120:121]
	v_add_f32_e32 v30, v33, v30
	v_pk_fma_f32 v[34:35], v[34:35], v[34:35], v[120:121]
	v_add_f32_e32 v30, v32, v30
	v_add_f32_e32 v30, v35, v30
	v_add_f32_e32 v30, v34, v30
	v_add_f32_e32 v30, v37, v30
	v_add_f32_e32 v30, v36, v30
	v_add_f32_e32 v30, v108, v30
	v_add_f32_e32 v30, v109, v30
	v_add_f32_e32 v30, v110, v30
	v_add_f32_e32 v30, v111, v30
	ds_bpermute_b32 v31, v207, v30
	s_waitcnt lgkmcnt(0)
	v_add_f32_e32 v30, v30, v31
	v_fmamk_f32 v30, v30, 0x3c000000, v198
	v_mul_f32_e32 v31, 0x4b800000, v30
	v_cmp_gt_f32_e32 vcc, s30, v30
	s_nop 1
	v_cndmask_b32_e32 v30, v30, v31, vcc
	v_rsq_f32_e32 v30, v30
	s_nop 0
	v_mul_f32_e32 v31, 0x45800000, v30
	v_cndmask_b32_e32 v30, v30, v31, vcc
	v_mul_f32_e32 v34, 0x3e0293ee, v30
	v_pk_mul_f32 v[30:31], v[34:35], v[44:45] op_sel_hi:[0,1]
	v_pk_mul_f32 v[32:33], v[34:35], v[42:43] op_sel_hi:[0,1]
	v_pk_mul_f32 v[30:31], v[132:133], v[30:31]
	v_pk_mul_f32 v[32:33], v[130:131], v[32:33]
	v_cvt_pk_bf16_f32 v30, v30, v31
	v_cvt_pk_bf16_f32 v31, v32, v33
	v_pk_mul_f32 v[32:33], v[34:35], v[40:41] op_sel_hi:[0,1]
	v_pk_mul_f32 v[36:37], v[34:35], v[38:39] op_sel_hi:[0,1]
	v_pk_mul_f32 v[32:33], v[136:137], v[32:33]
	v_pk_mul_f32 v[36:37], v[134:135], v[36:37]
	v_cvt_pk_bf16_f32 v32, v32, v33
	v_cvt_pk_bf16_f32 v33, v36, v37
	ds_write_b128 v233, v[30:33]
	v_pk_mul_f32 v[30:31], v[34:35], v[52:53] op_sel_hi:[0,1]
	v_pk_mul_f32 v[32:33], v[34:35], v[50:51] op_sel_hi:[0,1]
	v_pk_mul_f32 v[30:31], v[140:141], v[30:31]
	v_pk_mul_f32 v[32:33], v[138:139], v[32:33]
	v_cvt_pk_bf16_f32 v30, v30, v31
	v_cvt_pk_bf16_f32 v31, v32, v33
	v_pk_mul_f32 v[32:33], v[34:35], v[48:49] op_sel_hi:[0,1]
	v_pk_mul_f32 v[36:37], v[34:35], v[46:47] op_sel_hi:[0,1]
	v_pk_mul_f32 v[32:33], v[144:145], v[32:33]
	v_pk_mul_f32 v[36:37], v[142:143], v[36:37]
	v_cvt_pk_bf16_f32 v32, v32, v33
	v_cvt_pk_bf16_f32 v33, v36, v37
	ds_write_b128 v233, v[30:33] offset:1024
	v_pk_mul_f32 v[30:31], v[34:35], v[60:61] op_sel_hi:[0,1]
	v_pk_mul_f32 v[32:33], v[34:35], v[58:59] op_sel_hi:[0,1]
	v_pk_mul_f32 v[30:31], v[148:149], v[30:31]
	v_pk_mul_f32 v[32:33], v[146:147], v[32:33]
	v_cvt_pk_bf16_f32 v30, v30, v31
	v_cvt_pk_bf16_f32 v31, v32, v33
	v_pk_mul_f32 v[32:33], v[34:35], v[56:57] op_sel_hi:[0,1]
	v_pk_mul_f32 v[36:37], v[34:35], v[54:55] op_sel_hi:[0,1]
	v_pk_mul_f32 v[32:33], v[152:153], v[32:33]
	v_pk_mul_f32 v[36:37], v[150:151], v[36:37]
	v_cvt_pk_bf16_f32 v32, v32, v33
	v_cvt_pk_bf16_f32 v33, v36, v37
	ds_write_b128 v233, v[30:33] offset:2048
	v_pk_mul_f32 v[30:31], v[34:35], v[68:69] op_sel_hi:[0,1]
	v_pk_mul_f32 v[32:33], v[34:35], v[66:67] op_sel_hi:[0,1]
	v_pk_mul_f32 v[30:31], v[156:157], v[30:31]
	v_pk_mul_f32 v[32:33], v[154:155], v[32:33]
	v_cvt_pk_bf16_f32 v30, v30, v31
	v_cvt_pk_bf16_f32 v31, v32, v33
	v_pk_mul_f32 v[32:33], v[34:35], v[64:65] op_sel_hi:[0,1]
	v_pk_mul_f32 v[36:37], v[34:35], v[62:63] op_sel_hi:[0,1]
	v_pk_mul_f32 v[32:33], v[160:161], v[32:33]
	v_pk_mul_f32 v[36:37], v[158:159], v[36:37]
	v_cvt_pk_bf16_f32 v32, v32, v33
	v_cvt_pk_bf16_f32 v33, v36, v37
	v_lshl_or_b32 v36, s36, 19, v232
	v_mov_b32_e32 v37, v1
	v_lshl_add_u64 v[36:37], v[204:205], 0, v[36:37]
	v_add_co_u32_e32 v38, vcc, s31, v36
	ds_write_b128 v233, v[30:33] offset:3072
	s_nop 0
	v_addc_co_u32_e32 v39, vcc, 0, v37, vcc
	v_pk_mul_f32 v[30:31], v[34:35], v[114:115] op_sel_hi:[0,1]
	s_waitcnt vmcnt(0)
	v_mov_b64_e32 v[112:113], v[240:241]
	v_mov_b64_e32 v[114:115], v[242:243]
	v_mov_b64_e32 v[116:117], v[244:245]
	v_mov_b64_e32 v[118:119], v[246:247]
	v_add_co_u32_e32 v38, vcc, 0x40000, v36
	v_pk_mul_f32 v[32:33], v[34:35], v[70:71] op_sel_hi:[0,1]
	s_nop 0
	v_addc_co_u32_e32 v39, vcc, 0, v37, vcc
	v_add_co_u32_e32 v36, vcc, 0x41000, v36
	v_pk_mul_f32 v[12:13], v[34:35], v[12:13] op_sel_hi:[0,1]
	s_nop 0
	v_addc_co_u32_e32 v37, vcc, 0, v37, vcc
	v_mov_b64_e32 v[120:121], v[252:253]
	v_mov_b64_e32 v[122:123], v[254:255]
	v_mov_b64_e32 v[124:125], v[236:237]
	v_mov_b64_e32 v[126:127], v[238:239]
	v_pk_mul_f32 v[10:11], v[34:35], v[10:11] op_sel_hi:[0,1]
	v_pk_mul_f32 v[30:31], v[164:165], v[30:31]
	v_pk_mul_f32 v[32:33], v[162:163], v[32:33]
	v_pk_mul_f32 v[12:13], v[168:169], v[12:13]
	v_pk_mul_f32 v[10:11], v[166:167], v[10:11]
	v_cvt_pk_bf16_f32 v30, v30, v31
	v_cvt_pk_bf16_f32 v31, v32, v33
	v_cvt_pk_bf16_f32 v32, v12, v13
	v_cvt_pk_bf16_f32 v33, v10, v11
	v_pk_mul_f32 v[10:11], v[34:35], v[24:25] op_sel_hi:[0,1]
	v_pk_mul_f32 v[12:13], v[34:35], v[22:23] op_sel_hi:[0,1]
	v_pk_mul_f32 v[10:11], v[172:173], v[10:11]
	v_pk_mul_f32 v[12:13], v[170:171], v[12:13]
	v_cvt_pk_bf16_f32 v10, v10, v11
	v_cvt_pk_bf16_f32 v11, v12, v13
	v_pk_mul_f32 v[12:13], v[34:35], v[16:17] op_sel_hi:[0,1]
	v_pk_mul_f32 v[14:15], v[34:35], v[14:15] op_sel_hi:[0,1]
	v_pk_mul_f32 v[12:13], v[176:177], v[12:13]
	v_pk_mul_f32 v[14:15], v[174:175], v[14:15]
	v_cvt_pk_bf16_f32 v12, v12, v13
	v_cvt_pk_bf16_f32 v13, v14, v15
	ds_write_b128 v233, v[10:13] offset:5120
	v_pk_mul_f32 v[10:11], v[34:35], v[28:29] op_sel_hi:[0,1]
	v_pk_mul_f32 v[12:13], v[34:35], v[26:27] op_sel_hi:[0,1]
	v_pk_mul_f32 v[10:11], v[182:183], v[10:11]
	v_pk_mul_f32 v[12:13], v[180:181], v[12:13]
	v_cvt_pk_bf16_f32 v10, v10, v11
	v_cvt_pk_bf16_f32 v11, v12, v13
	v_pk_mul_f32 v[12:13], v[34:35], v[20:21] op_sel_hi:[0,1]
	v_pk_mul_f32 v[14:15], v[34:35], v[18:19] op_sel_hi:[0,1]
	v_pk_mul_f32 v[12:13], v[186:187], v[12:13]
	v_pk_mul_f32 v[14:15], v[184:185], v[14:15]
	v_cvt_pk_bf16_f32 v12, v12, v13
	v_cvt_pk_bf16_f32 v13, v14, v15
	ds_write_b128 v233, v[10:13] offset:6144
	v_mov_b32_e32 v11, v6
	v_mov_b32_e32 v6, v3
	v_pk_mul_f32 v[6:7], v[34:35], v[6:7] op_sel_hi:[0,1]
	v_pk_mul_f32 v[6:7], v[188:189], v[6:7]
	v_mov_b32_e32 v10, v2
	v_cvt_pk_bf16_f32 v3, v6, v7
	v_mov_b32_e32 v6, v4
	v_mov_b32_e32 v7, v8
	v_pk_mul_f32 v[6:7], v[34:35], v[6:7] op_sel_hi:[0,1]
	v_pk_mul_f32 v[6:7], v[194:195], v[6:7]
	v_mov_b32_e32 v8, v5
	v_pk_mul_f32 v[10:11], v[34:35], v[10:11] op_sel_hi:[0,1]
	v_cvt_pk_bf16_f32 v4, v6, v7
	v_pk_mul_f32 v[6:7], v[34:35], v[8:9] op_sel_hi:[0,1]
	v_pk_mul_f32 v[10:11], v[190:191], v[10:11]
	v_pk_mul_f32 v[6:7], v[192:193], v[6:7]
	v_cvt_pk_bf16_f32 v2, v10, v11
	v_cvt_pk_bf16_f32 v5, v6, v7
	v_mov_b32_e32 v14, v1
	v_mov_b32_e32 v15, v1
	ds_write_b128 v233, v[30:33] offset:4096
	ds_write_b128 v233, v[2:5] offset:7168
	v_mov_b32_e32 v2, v1
	v_mov_b32_e32 v3, v1
	v_mov_b32_e32 v4, v1
	v_mov_b32_e32 v5, v1
	v_mov_b32_e32 v6, v1
	v_mov_b32_e32 v7, v1
	v_mov_b32_e32 v8, v1
	v_mov_b32_e32 v9, v1
	v_mov_b32_e32 v10, v1
	v_mov_b32_e32 v11, v1
	v_mov_b32_e32 v12, v1
	v_mov_b32_e32 v13, v1
	v_mov_b64_e32 v[30:31], v[14:15]
	v_mov_b64_e32 v[46:47], v[14:15]
	v_mov_b64_e32 v[62:63], v[14:15]
	v_mov_b64_e32 v[78:79], v[14:15]
	v_mov_b64_e32 v[28:29], v[12:13]
	v_mov_b64_e32 v[26:27], v[10:11]
	v_mov_b64_e32 v[24:25], v[8:9]
	v_mov_b64_e32 v[22:23], v[6:7]
	v_mov_b64_e32 v[20:21], v[4:5]
	v_mov_b64_e32 v[18:19], v[2:3]
	v_mov_b64_e32 v[16:17], v[0:1]
	v_mov_b64_e32 v[44:45], v[12:13]
	v_mov_b64_e32 v[42:43], v[10:11]
	v_mov_b64_e32 v[40:41], v[8:9]
	v_mov_b64_e32 v[38:39], v[6:7]
	v_mov_b64_e32 v[36:37], v[4:5]
	v_mov_b64_e32 v[34:35], v[2:3]
	v_mov_b64_e32 v[32:33], v[0:1]
	v_mov_b64_e32 v[60:61], v[12:13]
	v_mov_b64_e32 v[58:59], v[10:11]
	v_mov_b64_e32 v[56:57], v[8:9]
	v_mov_b64_e32 v[54:55], v[6:7]
	v_mov_b64_e32 v[52:53], v[4:5]
	v_mov_b64_e32 v[50:51], v[2:3]
	v_mov_b64_e32 v[48:49], v[0:1]
	v_mov_b64_e32 v[76:77], v[12:13]
	v_mov_b64_e32 v[74:75], v[10:11]
	v_mov_b64_e32 v[72:73], v[8:9]
	v_mov_b64_e32 v[70:71], v[6:7]
	v_mov_b64_e32 v[68:69], v[4:5]
	v_mov_b64_e32 v[66:67], v[2:3]
	v_mov_b64_e32 v[64:65], v[0:1]
	s_branch .LBB0_297
